# MoE up/gate unit header: the four LIST lookups of the next unit issued together (one wait); prologue silu inputs loaded in one batch
# speedup vs baseline: 1.0115x; 1.0064x over previous
.LBB0_108:
	s_mov_b64 s[24:25], 0x1000
	v_lshl_add_u64 v[14:15], v[2:3], 0, s[24:25]
	v_lshl_add_u64 v[16:17], v[14:15], 0, s[24:25]
	v_lshl_add_u64 v[18:19], v[16:17], 0, s[24:25]
	v_add_u32_e32 v9, 0x1000, v6
	global_load_dword v20, v[2:3], off
	global_load_dword v21, v[2:3], off offset:2048
	global_load_dword v22, v[14:15], off
	global_load_dword v23, v[14:15], off offset:2048
	global_load_dword v24, v[16:17], off
	global_load_dword v25, v[16:17], off offset:2048
	global_load_dword v26, v[18:19], off
	global_load_dword v27, v[18:19], off offset:2048
	global_load_dword v28, v6, s[6:7]
	global_load_dword v29, v6, s[6:7] offset:2048
	global_load_dword v30, v9, s[6:7]
	global_load_dword v31, v9, s[6:7] offset:2048
	s_waitcnt vmcnt(11)
	v_mul_f32_e32 v8, 0xbfb8aa3b, v20
	v_exp_f32_e32 v8, v8
	s_nop 0
	v_add_f32_e32 v8, 1.0, v8
	v_div_scale_f32 v9, s[24:25], v8, v8, v20
	v_rcp_f32_e32 v10, v9
	v_div_scale_f32 v11, vcc, v20, v8, v20
	v_fma_f32 v12, -v9, v10, 1.0
	v_fmac_f32_e32 v10, v12, v10
	v_mul_f32_e32 v12, v11, v10
	v_fma_f32 v13, -v9, v12, v11
	v_fmac_f32_e32 v12, v13, v10
	v_fma_f32 v9, -v9, v12, v11
	v_div_fmas_f32 v9, v9, v10, v12
	v_div_fixup_f32 v4, v9, v8, v20
	ds_write_b32 v1, v4
	s_waitcnt vmcnt(10)
	v_mul_f32_e32 v8, 0xbfb8aa3b, v21
	v_exp_f32_e32 v8, v8
	s_nop 0
	v_add_f32_e32 v8, 1.0, v8
	v_div_scale_f32 v9, s[24:25], v8, v8, v21
	v_rcp_f32_e32 v10, v9
	v_div_scale_f32 v11, vcc, v21, v8, v21
	v_fma_f32 v12, -v9, v10, 1.0
	v_fmac_f32_e32 v10, v12, v10
	v_mul_f32_e32 v12, v11, v10
	v_fma_f32 v13, -v9, v12, v11
	v_fmac_f32_e32 v12, v13, v10
	v_fma_f32 v9, -v9, v12, v11
	v_div_fmas_f32 v9, v9, v10, v12
	v_div_fixup_f32 v4, v9, v8, v21
	ds_write_b32 v1, v4 offset:2048
	s_waitcnt vmcnt(9)
	v_mul_f32_e32 v8, 0xbfb8aa3b, v22
	v_exp_f32_e32 v8, v8
	s_nop 0
	v_add_f32_e32 v8, 1.0, v8
	v_div_scale_f32 v9, s[24:25], v8, v8, v22
	v_rcp_f32_e32 v10, v9
	v_div_scale_f32 v11, vcc, v22, v8, v22
	v_fma_f32 v12, -v9, v10, 1.0
	v_fmac_f32_e32 v10, v12, v10
	v_mul_f32_e32 v12, v11, v10
	v_fma_f32 v13, -v9, v12, v11
	v_fmac_f32_e32 v12, v13, v10
	v_fma_f32 v9, -v9, v12, v11
	v_div_fmas_f32 v9, v9, v10, v12
	v_div_fixup_f32 v4, v9, v8, v22
	ds_write_b32 v1, v4 offset:4096
	s_waitcnt vmcnt(8)
	v_mul_f32_e32 v8, 0xbfb8aa3b, v23
	v_exp_f32_e32 v8, v8
	s_nop 0
	v_add_f32_e32 v8, 1.0, v8
	v_div_scale_f32 v9, s[24:25], v8, v8, v23
	v_rcp_f32_e32 v10, v9
	v_div_scale_f32 v11, vcc, v23, v8, v23
	v_fma_f32 v12, -v9, v10, 1.0
	v_fmac_f32_e32 v10, v12, v10
	v_mul_f32_e32 v12, v11, v10
	v_fma_f32 v13, -v9, v12, v11
	v_fmac_f32_e32 v12, v13, v10
	v_fma_f32 v9, -v9, v12, v11
	v_div_fmas_f32 v9, v9, v10, v12
	v_div_fixup_f32 v4, v9, v8, v23
	ds_write_b32 v1, v4 offset:6144
	s_waitcnt vmcnt(7)
	v_mul_f32_e32 v8, 0xbfb8aa3b, v24
	v_exp_f32_e32 v8, v8
	s_nop 0
	v_add_f32_e32 v8, 1.0, v8
	v_div_scale_f32 v9, s[24:25], v8, v8, v24
	v_rcp_f32_e32 v10, v9
	v_div_scale_f32 v11, vcc, v24, v8, v24
	v_fma_f32 v12, -v9, v10, 1.0
	v_fmac_f32_e32 v10, v12, v10
	v_mul_f32_e32 v12, v11, v10
	v_fma_f32 v13, -v9, v12, v11
	v_fmac_f32_e32 v12, v13, v10
	v_fma_f32 v9, -v9, v12, v11
	v_div_fmas_f32 v9, v9, v10, v12
	v_div_fixup_f32 v4, v9, v8, v24
	ds_write_b32 v1, v4 offset:8192
	s_waitcnt vmcnt(6)
	v_mul_f32_e32 v8, 0xbfb8aa3b, v25
	v_exp_f32_e32 v8, v8
	s_nop 0
	v_add_f32_e32 v8, 1.0, v8
	v_div_scale_f32 v9, s[24:25], v8, v8, v25
	v_rcp_f32_e32 v10, v9
	v_div_scale_f32 v11, vcc, v25, v8, v25
	v_fma_f32 v12, -v9, v10, 1.0
	v_fmac_f32_e32 v10, v12, v10
	v_mul_f32_e32 v12, v11, v10
	v_fma_f32 v13, -v9, v12, v11
	v_fmac_f32_e32 v12, v13, v10
	v_fma_f32 v9, -v9, v12, v11
	v_div_fmas_f32 v9, v9, v10, v12
	v_div_fixup_f32 v4, v9, v8, v25
	ds_write_b32 v1, v4 offset:10240
	s_waitcnt vmcnt(5)
	v_mul_f32_e32 v8, 0xbfb8aa3b, v26
	v_exp_f32_e32 v8, v8
	s_nop 0
	v_add_f32_e32 v8, 1.0, v8
	v_div_scale_f32 v9, s[24:25], v8, v8, v26
	v_rcp_f32_e32 v10, v9
	v_div_scale_f32 v11, vcc, v26, v8, v26
	v_fma_f32 v12, -v9, v10, 1.0
	v_fmac_f32_e32 v10, v12, v10
	v_mul_f32_e32 v12, v11, v10
	v_fma_f32 v13, -v9, v12, v11
	v_fmac_f32_e32 v12, v13, v10
	v_fma_f32 v9, -v9, v12, v11
	v_div_fmas_f32 v9, v9, v10, v12
	v_div_fixup_f32 v4, v9, v8, v26
	ds_write_b32 v1, v4 offset:12288
	s_waitcnt vmcnt(4)
	v_mul_f32_e32 v8, 0xbfb8aa3b, v27
	v_exp_f32_e32 v8, v8
	s_nop 0
	v_add_f32_e32 v8, 1.0, v8
	v_div_scale_f32 v9, s[24:25], v8, v8, v27
	v_rcp_f32_e32 v10, v9
	v_div_scale_f32 v11, vcc, v27, v8, v27
	v_fma_f32 v12, -v9, v10, 1.0
	v_fmac_f32_e32 v10, v12, v10
	v_mul_f32_e32 v12, v11, v10
	v_fma_f32 v13, -v9, v12, v11
	v_fmac_f32_e32 v12, v13, v10
	v_fma_f32 v9, -v9, v12, v11
	v_div_fmas_f32 v9, v9, v10, v12
	v_div_fixup_f32 v4, v9, v8, v27
	ds_write_b32 v1, v4 offset:14336
	s_waitcnt vmcnt(3)
	v_mul_f32_e32 v8, 0xbfb8aa3b, v28
	v_exp_f32_e32 v8, v8
	s_nop 0
	v_add_f32_e32 v8, 1.0, v8
	v_div_scale_f32 v9, s[24:25], v8, v8, v28
	v_rcp_f32_e32 v10, v9
	v_div_scale_f32 v11, vcc, v28, v8, v28
	v_fma_f32 v12, -v9, v10, 1.0
	v_fmac_f32_e32 v10, v12, v10
	v_mul_f32_e32 v12, v11, v10
	v_fma_f32 v13, -v9, v12, v11
	v_fmac_f32_e32 v12, v13, v10
	v_fma_f32 v9, -v9, v12, v11
	v_div_fmas_f32 v9, v9, v10, v12
	v_div_fixup_f32 v4, v9, v8, v28
	ds_write_b32 v1, v4 offset:16384
	s_waitcnt vmcnt(2)
	v_mul_f32_e32 v8, 0xbfb8aa3b, v29
	v_exp_f32_e32 v8, v8
	s_nop 0
	v_add_f32_e32 v8, 1.0, v8
	v_div_scale_f32 v9, s[24:25], v8, v8, v29
	v_rcp_f32_e32 v10, v9
	v_div_scale_f32 v11, vcc, v29, v8, v29
	v_fma_f32 v12, -v9, v10, 1.0
	v_fmac_f32_e32 v10, v12, v10
	v_mul_f32_e32 v12, v11, v10
	v_fma_f32 v13, -v9, v12, v11
	v_fmac_f32_e32 v12, v13, v10
	v_fma_f32 v9, -v9, v12, v11
	v_div_fmas_f32 v9, v9, v10, v12
	v_div_fixup_f32 v4, v9, v8, v29
	ds_write_b32 v1, v4 offset:18432
	s_waitcnt vmcnt(1)
	v_mul_f32_e32 v8, 0xbfb8aa3b, v30
	v_exp_f32_e32 v8, v8
	s_nop 0
	v_add_f32_e32 v8, 1.0, v8
	v_div_scale_f32 v9, s[24:25], v8, v8, v30
	v_rcp_f32_e32 v10, v9
	v_div_scale_f32 v11, vcc, v30, v8, v30
	v_fma_f32 v12, -v9, v10, 1.0
	v_fmac_f32_e32 v10, v12, v10
	v_mul_f32_e32 v12, v11, v10
	v_fma_f32 v13, -v9, v12, v11
	v_fmac_f32_e32 v12, v13, v10
	v_fma_f32 v9, -v9, v12, v11
	v_div_fmas_f32 v9, v9, v10, v12
	v_div_fixup_f32 v4, v9, v8, v30
	ds_write_b32 v1, v4 offset:20480
	s_waitcnt vmcnt(0)
	v_mul_f32_e32 v8, 0xbfb8aa3b, v31
	v_exp_f32_e32 v8, v8
	s_nop 0
	v_add_f32_e32 v8, 1.0, v8
	v_div_scale_f32 v9, s[24:25], v8, v8, v31
	v_rcp_f32_e32 v10, v9
	v_div_scale_f32 v11, vcc, v31, v8, v31
	v_fma_f32 v12, -v9, v10, 1.0
	v_fmac_f32_e32 v10, v12, v10
	v_mul_f32_e32 v12, v11, v10
	v_fma_f32 v13, -v9, v12, v11
	v_fmac_f32_e32 v12, v13, v10
	v_fma_f32 v9, -v9, v12, v11
	v_div_fmas_f32 v9, v9, v10, v12
	v_div_fixup_f32 v4, v9, v8, v31
	ds_write_b32 v1, v4 offset:22528
	s_or_b64 exec, exec, s[8:9]

.LBB0_1847:
	v_lshlrev_b32_e32 v2, 2, v211
	v_add_u32_e32 v2, 0, v2
	v_cndmask_b32_e64 v4, 0, 1, s[8:9]
	v_add_u32_e32 v3, 0x20000, v2
	v_mul_lo_u32 v2, v211, s75
	v_cmp_ne_u32_e64 s[6:7], 1, v4
	s_andn2_b64 vcc, exec, s[8:9]
	v_mov_b32_e32 v212, v195
	v_mov_b32_e32 v213, v218
	v_mov_b32_e32 v214, v217
	v_mov_b32_e32 v215, v219
	s_cbranch_vccnz .LBB0_1855
	ds_read2_b32 v[4:5], v3 offset1:16
	s_waitcnt lgkmcnt(0)
	v_sub_u32_e32 v5, s76, v5
	v_add_u32_e32 v4, -1, v4
	v_lshl_add_u32 v14, v5, 8, v1
	v_min_i32_e32 v14, v14, v4
	v_add_u32_e32 v14, v14, v2
	v_ashrrev_i32_e32 v15, 31, v14
	v_lshl_add_u64 v[14:15], v[14:15], 2, s[26:27]
	v_lshl_add_u32 v16, v5, 8, v197
	v_min_i32_e32 v16, v16, v4
	v_add_u32_e32 v16, v16, v2
	v_ashrrev_i32_e32 v17, 31, v16
	v_lshl_add_u64 v[16:17], v[16:17], 2, s[26:27]
	v_lshl_add_u32 v18, v5, 8, v196
	v_min_i32_e32 v18, v18, v4
	v_add_u32_e32 v18, v18, v2
	v_ashrrev_i32_e32 v19, 31, v18
	v_lshl_add_u64 v[18:19], v[18:19], 2, s[26:27]
	v_lshl_add_u32 v20, v5, 8, v198
	v_min_i32_e32 v20, v20, v4
	v_add_u32_e32 v20, v20, v2
	v_ashrrev_i32_e32 v21, 31, v20
	v_lshl_add_u64 v[20:21], v[20:21], 2, s[26:27]
	global_load_dword v10, v[14:15], off
	global_load_dword v11, v[16:17], off
	global_load_dword v12, v[18:19], off
	global_load_dword v13, v[20:21], off
	s_waitcnt vmcnt(0)
	v_lshlrev_b32_e32 v10, 10, v10
	v_and_b32_e32 v10, 0xfffff800, v10
	v_add_u32_e32 v212, v10, v199
	v_lshlrev_b32_e32 v11, 10, v11
	v_and_b32_e32 v11, 0xfffff800, v11
	v_add_u32_e32 v213, v11, v199
	v_lshlrev_b32_e32 v12, 10, v12
	v_and_b32_e32 v12, 0xfffff800, v12
	v_add_u32_e32 v214, v12, v201
	v_lshlrev_b32_e32 v13, 10, v13
	v_and_b32_e32 v13, 0xfffff800, v13
	v_add_u32_e32 v215, v13, v201
